# al1: code placement: the GEMM k-loop heads (IN, chain stages, MoE) and the two attention tile-loop heads aligned to 64 bytes (.p2align 6); on top of cv1
# speedup vs baseline: 1.0001x; 1.0001x over previous
; template <class Epi, class Sched, bool GATHER, bool ALIGN_EPI>
; __device__ __forceinline__ void gemm_phase(LAS unsigned char* lds, const int wave_, const int K, const int lda, const int ldb, const Sched& S, const Epi& E) {
;     ...
;         for (int t = 0; t < nt; t += 2) {
;             const bool last = (t == nt - 2);
;             const char* a1 = cA + (size_t)(t + 1) * kstep;
;             const char* a2 = last ? nA : cA + (size_t)(t + 2) * kstep; const char* b2 = last ? nB : cB + (size_t)(t + 2) * kstep;
;     ...
;         if (!keep) {
; #pragma unroll
;             for (int a = 0; a < 2; ++a)
; #pragma unroll
;                 for (int b = 0; b < 2; ++b)
; #pragma unroll
;                     for (int m = 0; m < 4; ++m)
; #pragma unroll
;                         for (int n = 0; n < 2; ++n) acc[a][b][m][n] = (f32x4){0.f, 0.f, 0.f, 0.f};
.LBB0_719:
	s_add_u32 s4, s4, 0x40080
	s_addc_u32 s5, s5, 0
	s_add_u32 s11, s18, 0x100
	v_mov_b32_e32 v0, 0
	v_mov_b64_e32 v[210:211], 0xff
	s_addc_u32 s13, s19, 0
	s_mov_b32 s31, -2
	v_mov_b32_e32 v1, v0
	v_mov_b32_e32 v2, v0
	v_mov_b32_e32 v3, v0
	v_mov_b32_e32 v4, v0
	v_mov_b32_e32 v5, v0
	v_mov_b32_e32 v6, v0
	v_mov_b32_e32 v7, v0
	v_mov_b32_e32 v16, v0
	v_mov_b32_e32 v17, v0
	v_mov_b32_e32 v18, v0
	v_mov_b32_e32 v19, v0
	v_mov_b32_e32 v20, v0
	v_mov_b32_e32 v21, v0
	v_mov_b32_e32 v22, v0
	v_mov_b32_e32 v23, v0
	v_mov_b32_e32 v32, v0
	v_mov_b32_e32 v33, v0
	v_mov_b32_e32 v34, v0
	v_mov_b32_e32 v35, v0
	v_mov_b32_e32 v36, v0
	v_mov_b32_e32 v37, v0
	v_mov_b32_e32 v38, v0
	v_mov_b32_e32 v39, v0
	v_mov_b32_e32 v48, v0
	v_mov_b32_e32 v49, v0
	v_mov_b32_e32 v50, v0
	v_mov_b32_e32 v51, v0
	v_mov_b32_e32 v52, v0
	v_mov_b32_e32 v53, v0
	v_mov_b32_e32 v54, v0
	v_mov_b32_e32 v55, v0
	v_mov_b32_e32 v8, v0
	v_mov_b32_e32 v9, v0
	v_mov_b32_e32 v10, v0
	v_mov_b32_e32 v11, v0
	v_mov_b32_e32 v12, v0
	v_mov_b32_e32 v13, v0
	v_mov_b32_e32 v14, v0
	v_mov_b32_e32 v15, v0
	v_mov_b32_e32 v24, v0
	v_mov_b32_e32 v25, v0
	v_mov_b32_e32 v26, v0
	v_mov_b32_e32 v27, v0
	v_mov_b32_e32 v28, v0
	v_mov_b32_e32 v29, v0
	v_mov_b32_e32 v30, v0
	v_mov_b32_e32 v31, v0
	v_mov_b32_e32 v40, v0
	v_mov_b32_e32 v41, v0
	v_mov_b32_e32 v42, v0
	v_mov_b32_e32 v43, v0
	v_mov_b32_e32 v44, v0
	v_mov_b32_e32 v45, v0
	v_mov_b32_e32 v46, v0
	v_mov_b32_e32 v47, v0
	v_mov_b32_e32 v56, v0
	v_mov_b32_e32 v57, v0
	v_mov_b32_e32 v58, v0
	v_mov_b32_e32 v59, v0
	v_mov_b32_e32 v60, v0
	v_mov_b32_e32 v61, v0
	v_mov_b32_e32 v62, v0
	v_mov_b32_e32 v63, v0
	v_mov_b32_e32 v64, v0
	v_mov_b32_e32 v65, v0
	v_mov_b32_e32 v66, v0
	v_mov_b32_e32 v67, v0
	v_mov_b32_e32 v68, v0
	v_mov_b32_e32 v69, v0
	v_mov_b32_e32 v70, v0
	v_mov_b32_e32 v71, v0
	v_mov_b32_e32 v80, v0
	v_mov_b32_e32 v81, v0
	v_mov_b32_e32 v82, v0
	v_mov_b32_e32 v83, v0
	v_mov_b32_e32 v84, v0
	v_mov_b32_e32 v85, v0
	v_mov_b32_e32 v86, v0
	v_mov_b32_e32 v87, v0
	v_mov_b32_e32 v96, v0
	v_mov_b32_e32 v97, v0
	v_mov_b32_e32 v98, v0
	v_mov_b32_e32 v99, v0
	v_mov_b32_e32 v100, v0
	v_mov_b32_e32 v101, v0
	v_mov_b32_e32 v102, v0
	v_mov_b32_e32 v103, v0
	v_mov_b32_e32 v112, v0
	v_mov_b32_e32 v113, v0
	v_mov_b32_e32 v114, v0
	v_mov_b32_e32 v115, v0
	v_mov_b32_e32 v116, v0
	v_mov_b32_e32 v117, v0
	v_mov_b32_e32 v118, v0
	v_mov_b32_e32 v119, v0
	v_mov_b32_e32 v72, v0
	v_mov_b32_e32 v73, v0
	v_mov_b32_e32 v74, v0
	v_mov_b32_e32 v75, v0
	v_mov_b32_e32 v76, v0
	v_mov_b32_e32 v77, v0
	v_mov_b32_e32 v78, v0
	v_mov_b32_e32 v79, v0
	v_mov_b32_e32 v88, v0
	v_mov_b32_e32 v89, v0
	v_mov_b32_e32 v90, v0
	v_mov_b32_e32 v91, v0
	v_mov_b32_e32 v92, v0
	v_mov_b32_e32 v93, v0
	v_mov_b32_e32 v94, v0
	v_mov_b32_e32 v95, v0
	v_mov_b32_e32 v104, v0
	v_mov_b32_e32 v105, v0
	v_mov_b32_e32 v106, v0
	v_mov_b32_e32 v107, v0
	v_mov_b32_e32 v108, v0
	v_mov_b32_e32 v109, v0
	v_mov_b32_e32 v110, v0
	v_mov_b32_e32 v111, v0
	v_mov_b32_e32 v120, v0
	v_mov_b32_e32 v121, v0
	v_mov_b32_e32 v122, v0
	v_mov_b32_e32 v123, v0
	v_mov_b32_e32 v124, v0
	v_mov_b32_e32 v125, v0
	v_mov_b32_e32 v126, v0
	v_mov_b32_e32 v127, v0
	.p2align	6

; #define SBAR() __builtin_amdgcn_sched_barrier(0)
; #define SLOAD(k0) do { vs0 = *reinterpret_cast<const bf16x8*>(&Vh[(size_t)((k0) + sr) * DM + sc]); vs1 = *reinterpret_cast<const bf16x8*>(&Vh[(size_t)((k0) + 32 + sr) * DM + sc]); \
;     ks = *reinterpret_cast<const bf16x8*>(&Kh[(size_t)((k0) + kr) * DM + kc]); } while (0)
; __device__ __forceinline__ void diff_pass(const bf16_t* __restrict__ Qb, const bf16_t* __restrict__ Kh, const bf16_t* __restrict__ Vh, int seq, char* lds, f32x16 (&o)[4], const int wave_) {
;     ...
;     for (int j = 1; j + 1 < NT; j += 2) {
;         SLOAD((j + 1) * 64);
;         SBAR(); qkt64c(pB0, pB1, K_lds + s_cur * SHM_K64, qr, negm, r32, hi); FIN(pA0, pA1, alA); SBAR();
.LBB0_823:
	s_lshl_b32 s2, s42, 13
	s_add_i32 s2, s2, 0
	v_add_u32_e32 v128, s2, v223
	v_add_u32_e32 v129, s2, v226
	v_add_u32_e32 v130, s2, v228
	v_add_u32_e32 v131, s2, v229
	.p2align	6

; #define SBAR() __builtin_amdgcn_sched_barrier(0)
; #define SLOAD(k0) do { vs0 = *reinterpret_cast<const bf16x8*>(&Vh[(size_t)((k0) + sr) * DM + sc]); vs1 = *reinterpret_cast<const bf16x8*>(&Vh[(size_t)((k0) + 32 + sr) * DM + sc]); \
;     ks = *reinterpret_cast<const bf16x8*>(&Kh[(size_t)((k0) + kr) * DM + kc]); } while (0)
; __device__ __forceinline__ void diff_pass(const bf16_t* __restrict__ Qb, const bf16_t* __restrict__ Kh, const bf16_t* __restrict__ Vh, int seq, char* lds, f32x16 (&o)[4], const int wave_) {
;     ...
;         SLOAD((j + 2) * 64);
;         SBAR(); qkt64c(pA0, pA1, K_lds + s_cur * SHM_K64, qr, negm, r32, hi); FIN(pB0, pB1, alB); SBAR();
.LBB0_846:
	s_lshl_b32 s2, s30, 13
	s_add_i32 s2, s2, 0
	v_add_u32_e32 v128, s2, v227
	v_add_u32_e32 v129, s2, v231
	v_add_u32_e32 v130, s2, v232
	v_add_u32_e32 v131, s2, v233
	.p2align	6

; template <class Epi, class Sched, bool GATHER, bool ALIGN_EPI>
; __device__ __forceinline__ void gemm_phase(LAS unsigned char* lds, const int wave_, const int K, const int lda, const int ldb, const Sched& S, const Epi& E) {
;     ...
;         const char* nA = has_next ? nxt.A : cA; const char* nB = has_next ? nxt.B : cB;
;         for (int t = 0; t < nt; t += 2) {
;             const bool last = (t == nt - 2);
;             const char* a1 = cA + (size_t)(t + 1) * kstep;
;             const char* a2 = last ? nA : cA + (size_t)(t + 2) * kstep; const char* b2 = last ? nB : cB + (size_t)(t + 2) * kstep;
;             const char* a3 = a2 + kstep; const char* b3 = b2 + kstep;
.LBB0_932:
	s_and_b64 s[2:3], s[10:11], exec
	s_cselect_b32 s2, s17, s21
	s_cselect_b32 s3, s16, s20
	s_cselect_b32 s5, s19, s13
	s_cselect_b32 s8, s18, s12
	s_add_u32 s20, s20, 0x40080
	s_addc_u32 s21, s21, 0
	s_add_u32 s9, s12, 0x100
	s_addc_u32 s15, s13, 0
	s_mov_b32 s40, -2
	.p2align	6

; #define PG8_STAGE(bufoff, gbase, voff) do { _Pragma("unroll") for (int _i = 0; _i < 2; ++_i) \
;         __builtin_amdgcn_global_load_lds((const unsigned*)((const char*)(gbase) + (voff)[_i]), (LAS unsigned*)(lds + (bufoff) + ldsw + _i * 8192), 16, 0, 0); } while (0)
; #define PG8_STAGE_A(bufoff, gbase, h, nx) do { if constexpr (GATHER) { unsigned _v[2]; _v[0] = (nx) ? voffAn[h][0] : voffA[h][0]; _v[1] = (nx) ? voffAn[h][1] : voffA[h][1]; PG8_STAGE(bufoff, gbase, _v); } \
;         else PG8_STAGE(bufoff, (gbase) + (h) * hstepA, voffA[0]); } while (0)
; #define PG8_WAIT_V(n) asm volatile("s_waitcnt vmcnt(" #n ")" ::: "memory")
; #define PG8_WAIT_L(n) asm volatile("s_waitcnt lgkmcnt(" #n ")" ::: "memory")
; template <class Epi, class Sched, bool GATHER, bool ALIGN_EPI>
; __device__ __forceinline__ void gemm_phase(LAS unsigned char* lds, const int wave_, const int K, const int lda, const int ldb, const Sched& S, const Epi& E) {
;     ...
;         for (int t = 0; t < nt; t += 2) {
;             const bool last = (t == nt - 2);
;             const char* a1 = cA + (size_t)(t + 1) * kstep;
;             const char* a2 = last ? nA : cA + (size_t)(t + 2) * kstep; const char* b2 = last ? nB : cB + (size_t)(t + 2) * kstep;
;             const char* a3 = a2 + kstep; const char* b3 = b2 + kstep;
;             if (last && has_next) S.a_ready(nxt);
;             PG8_LDB(B0, 0, 0); PG8_LDB(B1, 0, 1); PG8_SCHED; PG8_LDA(At, 0, 0); PG8_STAGE_A(PG8_SA(1, 1), a1, 1, false);
;             PG8_WAIT_V(8); PG8_WAIT_L(0); PG8_BAR; PG8_MMA(0, 0, At, B0); PG8_MMA(0, 1, At, B1); PG8_BAR; PG8_SCHED;
;             PG8_LDA(At, 0, 1); PG8_STAGE(PG8_SB(0, 0), b2, voffB); PG8_STAGE(PG8_SB(0, 1), b2 + hstepB, voffB); PG8_STAGE_A(PG8_SA(0, 0), a2, 0, last);
;             PG8_WAIT_V(8); PG8_WAIT_L(0); PG8_BAR; PG8_MMA(1, 0, At, B0); PG8_MMA(1, 1, At, B1); PG8_BAR; PG8_SCHED;
;             PG8_LDB(B0, 1, 0); PG8_LDB(B1, 1, 1); PG8_SCHED; PG8_LDA(At, 1, 0); PG8_STAGE_A(PG8_SA(0, 1), a2, 1, last);
;             PG8_WAIT_V(8); PG8_WAIT_L(0); PG8_BAR; PG8_MMA(0, 0, At, B0); PG8_MMA(0, 1, At, B1); PG8_BAR; PG8_SCHED;
;             PG8_LDA(At, 1, 1); PG8_STAGE(PG8_SB(1, 0), b3, voffB); PG8_STAGE(PG8_SB(1, 1), b3 + hstepB, voffB); PG8_STAGE_A(PG8_SA(1, 0), a3, 0, last);
;             PG8_WAIT_V(8); PG8_WAIT_L(0); PG8_BAR; PG8_MMA(1, 0, At, B0); PG8_MMA(1, 1, At, B1); PG8_BAR; PG8_SCHED;
.LBB0_1013:
	s_barrier
	.p2align	6

; #define PG8_STAGE(bufoff, gbase, voff) do { _Pragma("unroll") for (int _i = 0; _i < 2; ++_i) \
;         __builtin_amdgcn_global_load_lds((const unsigned*)((const char*)(gbase) + (voff)[_i]), (LAS unsigned*)(lds + (bufoff) + ldsw + _i * 8192), 16, 0, 0); } while (0)
; #define PG8_STAGE_A(bufoff, gbase, h, nx) do { if constexpr (GATHER) { unsigned _v[2]; _v[0] = (nx) ? voffAn[h][0] : voffA[h][0]; _v[1] = (nx) ? voffAn[h][1] : voffA[h][1]; PG8_STAGE(bufoff, gbase, _v); } \
;         else PG8_STAGE(bufoff, (gbase) + (h) * hstepA, voffA[0]); } while (0)
; #define PG8_LDA(dst, b, h) do { _Pragma("unroll") for (int m = 0; m < 4; ++m) _Pragma("unroll") for (int k = 0; k < 2; ++k) dst[m][k] = *(const LAS bf16x8*)(lds + PG8_SA(b, h) + aoff + m * 2048 + k * 1024); } while (0)
; #define PG8_LDB(dst, b, h) do { _Pragma("unroll") for (int n = 0; n < 2; ++n) _Pragma("unroll") for (int k = 0; k < 2; ++k) dst[n][k] = *(const LAS bf16x8*)(lds + PG8_SB(b, h) + boff + n * 2048 + k * 1024); } while (0)
; #define PG8_WAIT_V(n) asm volatile("s_waitcnt vmcnt(" #n ")" ::: "memory")
; #define PG8_WAIT_L(n) asm volatile("s_waitcnt lgkmcnt(" #n ")" ::: "memory")
; #define PG8_BAR __builtin_amdgcn_s_barrier()
; #define PG8_SCHED __builtin_amdgcn_sched_barrier(0)
; template <class Epi, class Sched, bool GATHER, bool ALIGN_EPI>
; __device__ __forceinline__ void gemm_phase(LAS unsigned char* lds, const int wave_, const int K, const int lda, const int ldb, const Sched& S, const Epi& E) {
;     ...
;         const char* nA = has_next ? nxt.A : cA; const char* nB = has_next ? nxt.B : cB;
;         for (int t = 0; t < nt; t += 2) {
;             const bool last = (t == nt - 2);
;             const char* a1 = cA + (size_t)(t + 1) * kstep;
;             const char* a2 = last ? nA : cA + (size_t)(t + 2) * kstep; const char* b2 = last ? nB : cB + (size_t)(t + 2) * kstep;
;             const char* a3 = a2 + kstep; const char* b3 = b2 + kstep;
;             if (last && has_next) S.a_ready(nxt);
;             PG8_LDB(B0, 0, 0); PG8_LDB(B1, 0, 1); PG8_SCHED; PG8_LDA(At, 0, 0); PG8_STAGE_A(PG8_SA(1, 1), a1, 1, false);
;             PG8_WAIT_V(8); PG8_WAIT_L(0); PG8_BAR; PG8_MMA(0, 0, At, B0); PG8_MMA(0, 1, At, B1); PG8_BAR; PG8_SCHED;
;             PG8_LDA(At, 0, 1); PG8_STAGE(PG8_SB(0, 0), b2, voffB); PG8_STAGE(PG8_SB(0, 1), b2 + hstepB, voffB); PG8_STAGE_A(PG8_SA(0, 0), a2, 0, last);
.LBB0_1495:
	s_add_u32 s15, s4, 0x100
	s_addc_u32 s49, s5, 0
	s_add_u32 s2, s12, 0x80
	v_mov_b32_e32 v165, v161
	v_mov_b32_e32 v173, v161
	s_addc_u32 s3, s13, 0
	v_mov_b64_e32 v[184:185], 0xff
	v_mov_b64_e32 v[246:247], 0x100
	v_lshl_add_u64 v[128:129], s[2:3], 0, v[172:173]
	v_lshl_add_u64 v[130:131], s[2:3], 0, v[164:165]
	s_mov_b32 s50, -2
	s_mov_b64 s[4:5], 0
	.p2align	6

;     __device__ __forceinline__ void a_ready(const pg8::Unit& u) const { if (ready) wg_wait_counter(ready + 64 * u.pm, need, tmo, wave); }
;     __device__ __forceinline__ void a_ready(const pg8::Unit& u) const { d.a_ready(u); }
;     __device__ __forceinline__ void a_ready(const pg8::Unit& u) const {
;         if (!ready) return;
;         if (wave == 0) {
;             const unsigned long long t0 = __builtin_amdgcn_s_memrealtime(); unsigned polls = 0;
;             while ((unsigned)__builtin_amdgcn_readfirstlane(__hip_atomic_load(ready + 64 * u.pm, __ATOMIC_RELAXED, __HIP_MEMORY_SCOPE_AGENT)) < need) {
.LBB0_1557:
	s_lshl_b32 s2, s44, 6
	v_readlane_b32 s8, v253, 35
	s_ashr_i32 s3, s2, 31
	v_readlane_b32 s9, v253, 36
	s_or_b64 s[16:17], s[0:1], s[8:9]
	s_lshl_b64 s[2:3], s[2:3], 2
	s_add_u32 s18, s30, s2
	s_addc_u32 s19, s31, s3
	s_mov_b32 s46, 0
	.p2align	6
